# gather: counted vmcnt per LDS-DMA group (read each row group back as soon as its DMA landed) instead of draining all seven first
# baseline (speedup 1.0000x reference)
_Z13gather_kernelPKDv2_DF16_PKiPf:
	s_load_dwordx4 s[8:11], s[0:1], 0x0
	s_load_dwordx2 s[4:5], s[0:1], 0x10
	s_lshl_b32 s0, s2, 11
	s_and_b32 s0, s0, 0x3800
	s_lshr_b32 s1, s2, 3
	s_add_i32 s0, s0, s1
	v_lshrrev_b32_e32 v1, 6, v0
	v_and_b32_e32 v2, 63, v0
	v_readfirstlane_b32 s14, v1
	v_lshl_or_b32 v1, s0, 2, v1
	v_lshrrev_b32_e32 v3, 4, v2
	v_and_b32_e32 v4, 15, v2
	v_mul_u32_u24_e32 v5, 25, v1
	v_add_u32_e32 v6, v5, v3
	v_lshlrev_b32_e32 v6, 2, v6
	v_lshlrev_b32_e32 v7, 4, v4
	v_lshlrev_b32_e32 v14, 2, v5
	v_lshrrev_b32_e32 v17, 5, v2
	v_bfe_u32 v18, v2, 4, 1
	v_lshl_or_b32 v19, v17, 3, v7
	v_lshl_or_b32 v19, v18, 2, v19
	v_lshlrev_b32_e32 v46, 1, v19
	v_lshl_or_b32 v46, v1, 9, v46
	s_mul_i32 s14, s14, 7168
	v_lshlrev_b32_e32 v45, 4, v2
	v_add_u32_e32 v45, s14, v45
	v_lshlrev_b32_e32 v47, 2, v2
	v_add_u32_e32 v47, s14, v47
	s_mov_b32 s12, 0x3d23d70a
	s_waitcnt lgkmcnt(0)
	global_load_dword v8, v6, s[10:11]
	global_load_dword v9, v6, s[10:11] offset:16
	global_load_dword v10, v6, s[10:11] offset:32
	global_load_dword v11, v6, s[10:11] offset:48
	global_load_dword v12, v6, s[10:11] offset:64
	global_load_dword v13, v6, s[10:11] offset:80
	global_load_dword v15, v14, s[10:11] offset:96
	s_waitcnt vmcnt(6)
	v_lshl_or_b32 v16, v8, 8, v7
	s_add_u32 s15, s14, 0
	s_mov_b32 m0, s15
	s_nop 0
	global_load_lds_dwordx4 v16, s[8:9]
	s_waitcnt vmcnt(6)
	v_lshl_or_b32 v16, v9, 8, v7
	s_add_u32 s15, s14, 1024
	s_mov_b32 m0, s15
	s_nop 0
	global_load_lds_dwordx4 v16, s[8:9]
	s_waitcnt vmcnt(6)
	v_lshl_or_b32 v16, v10, 8, v7
	s_add_u32 s15, s14, 2048
	s_mov_b32 m0, s15
	s_nop 0
	global_load_lds_dwordx4 v16, s[8:9]
	s_waitcnt vmcnt(6)
	v_lshl_or_b32 v16, v11, 8, v7
	s_add_u32 s15, s14, 3072
	s_mov_b32 m0, s15
	s_nop 0
	global_load_lds_dwordx4 v16, s[8:9]
	s_waitcnt vmcnt(6)
	v_lshl_or_b32 v16, v12, 8, v7
	s_add_u32 s15, s14, 4096
	s_mov_b32 m0, s15
	s_nop 0
	global_load_lds_dwordx4 v16, s[8:9]
	s_waitcnt vmcnt(6)
	v_lshl_or_b32 v16, v13, 8, v7
	s_add_u32 s15, s14, 5120
	s_mov_b32 m0, s15
	s_nop 0
	global_load_lds_dwordx4 v16, s[8:9]
	s_waitcnt vmcnt(6)
	v_lshl_or_b32 v16, v15, 8, v19
	s_add_u32 s15, s14, 6144
	s_mov_b32 m0, s15
	s_nop 0
	global_load_lds_dword v16, s[8:9]
	s_waitcnt vmcnt(6)
	ds_read_b128 v[20:23], v45
	s_waitcnt vmcnt(5)
	ds_read_b128 v[24:27], v45 offset:1024
	s_waitcnt vmcnt(4)
	ds_read_b128 v[28:31], v45 offset:2048
	s_waitcnt vmcnt(3)
	ds_read_b128 v[32:35], v45 offset:3072
	s_waitcnt vmcnt(2)
	ds_read_b128 v[36:39], v45 offset:4096
	s_waitcnt vmcnt(1)
	ds_read_b128 v[40:43], v45 offset:5120
	s_waitcnt vmcnt(0)
	ds_read_b32 v44, v47 offset:6144
	s_waitcnt lgkmcnt(6)
	v_cvt_f32_f16_e32 v48, v20
	v_cvt_f32_f16_sdwa v49, v20 dst_sel:DWORD dst_unused:UNUSED_PAD src0_sel:WORD_1
	v_cvt_f32_f16_e32 v50, v21
	v_cvt_f32_f16_sdwa v51, v21 dst_sel:DWORD dst_unused:UNUSED_PAD src0_sel:WORD_1
	v_cvt_f32_f16_e32 v52, v22
	v_cvt_f32_f16_sdwa v53, v22 dst_sel:DWORD dst_unused:UNUSED_PAD src0_sel:WORD_1
	v_cvt_f32_f16_e32 v54, v23
	v_cvt_f32_f16_sdwa v55, v23 dst_sel:DWORD dst_unused:UNUSED_PAD src0_sel:WORD_1
	s_waitcnt lgkmcnt(5)
	v_cvt_f32_f16_e32 v56, v24
	v_cvt_f32_f16_sdwa v57, v24 dst_sel:DWORD dst_unused:UNUSED_PAD src0_sel:WORD_1
	v_cvt_f32_f16_e32 v58, v25
	v_cvt_f32_f16_sdwa v59, v25 dst_sel:DWORD dst_unused:UNUSED_PAD src0_sel:WORD_1
	v_cvt_f32_f16_e32 v60, v26
	v_cvt_f32_f16_sdwa v61, v26 dst_sel:DWORD dst_unused:UNUSED_PAD src0_sel:WORD_1
	v_cvt_f32_f16_e32 v62, v27
	v_cvt_f32_f16_sdwa v63, v27 dst_sel:DWORD dst_unused:UNUSED_PAD src0_sel:WORD_1
	v_pk_add_f32 v[48:49], v[48:49], v[56:57]
	v_pk_add_f32 v[50:51], v[50:51], v[58:59]
	v_pk_add_f32 v[52:53], v[52:53], v[60:61]
	v_pk_add_f32 v[54:55], v[54:55], v[62:63]
	s_waitcnt lgkmcnt(4)
	v_cvt_f32_f16_e32 v56, v28
	v_cvt_f32_f16_sdwa v57, v28 dst_sel:DWORD dst_unused:UNUSED_PAD src0_sel:WORD_1
	v_cvt_f32_f16_e32 v58, v29
	v_cvt_f32_f16_sdwa v59, v29 dst_sel:DWORD dst_unused:UNUSED_PAD src0_sel:WORD_1
	v_cvt_f32_f16_e32 v60, v30
	v_cvt_f32_f16_sdwa v61, v30 dst_sel:DWORD dst_unused:UNUSED_PAD src0_sel:WORD_1
	v_cvt_f32_f16_e32 v62, v31
	v_cvt_f32_f16_sdwa v63, v31 dst_sel:DWORD dst_unused:UNUSED_PAD src0_sel:WORD_1
	v_pk_add_f32 v[48:49], v[48:49], v[56:57]
	v_pk_add_f32 v[50:51], v[50:51], v[58:59]
	v_pk_add_f32 v[52:53], v[52:53], v[60:61]
	v_pk_add_f32 v[54:55], v[54:55], v[62:63]
	s_waitcnt lgkmcnt(3)
	v_cvt_f32_f16_e32 v56, v32
	v_cvt_f32_f16_sdwa v57, v32 dst_sel:DWORD dst_unused:UNUSED_PAD src0_sel:WORD_1
	v_cvt_f32_f16_e32 v58, v33
	v_cvt_f32_f16_sdwa v59, v33 dst_sel:DWORD dst_unused:UNUSED_PAD src0_sel:WORD_1
	v_cvt_f32_f16_e32 v60, v34
	v_cvt_f32_f16_sdwa v61, v34 dst_sel:DWORD dst_unused:UNUSED_PAD src0_sel:WORD_1
	v_cvt_f32_f16_e32 v62, v35
	v_cvt_f32_f16_sdwa v63, v35 dst_sel:DWORD dst_unused:UNUSED_PAD src0_sel:WORD_1
	v_pk_add_f32 v[48:49], v[48:49], v[56:57]
	v_pk_add_f32 v[50:51], v[50:51], v[58:59]
	v_pk_add_f32 v[52:53], v[52:53], v[60:61]
	v_pk_add_f32 v[54:55], v[54:55], v[62:63]
	s_waitcnt lgkmcnt(2)
	v_cvt_f32_f16_e32 v56, v36
	v_cvt_f32_f16_sdwa v57, v36 dst_sel:DWORD dst_unused:UNUSED_PAD src0_sel:WORD_1
	v_cvt_f32_f16_e32 v58, v37
	v_cvt_f32_f16_sdwa v59, v37 dst_sel:DWORD dst_unused:UNUSED_PAD src0_sel:WORD_1
	v_cvt_f32_f16_e32 v60, v38
	v_cvt_f32_f16_sdwa v61, v38 dst_sel:DWORD dst_unused:UNUSED_PAD src0_sel:WORD_1
	v_cvt_f32_f16_e32 v62, v39
	v_cvt_f32_f16_sdwa v63, v39 dst_sel:DWORD dst_unused:UNUSED_PAD src0_sel:WORD_1
	v_pk_add_f32 v[48:49], v[48:49], v[56:57]
	v_pk_add_f32 v[50:51], v[50:51], v[58:59]
	v_pk_add_f32 v[52:53], v[52:53], v[60:61]
	v_pk_add_f32 v[54:55], v[54:55], v[62:63]
	s_waitcnt lgkmcnt(1)
	v_cvt_f32_f16_e32 v56, v40
	v_cvt_f32_f16_sdwa v57, v40 dst_sel:DWORD dst_unused:UNUSED_PAD src0_sel:WORD_1
	v_cvt_f32_f16_e32 v58, v41
	v_cvt_f32_f16_sdwa v59, v41 dst_sel:DWORD dst_unused:UNUSED_PAD src0_sel:WORD_1
	v_cvt_f32_f16_e32 v60, v42
	v_cvt_f32_f16_sdwa v61, v42 dst_sel:DWORD dst_unused:UNUSED_PAD src0_sel:WORD_1
	v_cvt_f32_f16_e32 v62, v43
	v_cvt_f32_f16_sdwa v63, v43 dst_sel:DWORD dst_unused:UNUSED_PAD src0_sel:WORD_1
	v_pk_add_f32 v[48:49], v[48:49], v[56:57]
	v_pk_add_f32 v[50:51], v[50:51], v[58:59]
	v_pk_add_f32 v[52:53], v[52:53], v[60:61]
	v_pk_add_f32 v[54:55], v[54:55], v[62:63]
	s_waitcnt lgkmcnt(0)
	v_cvt_f32_f16_e32 v56, v44
	v_cvt_f32_f16_sdwa v57, v44 dst_sel:DWORD dst_unused:UNUSED_PAD src0_sel:WORD_1
	v_permlane32_swap_b32_e32 v48, v52
	v_permlane32_swap_b32_e32 v49, v53
	v_permlane32_swap_b32_e32 v50, v54
	v_permlane32_swap_b32_e32 v51, v55
	s_nop 0
	v_pk_add_f32 v[48:49], v[48:49], v[52:53]
	v_pk_add_f32 v[50:51], v[50:51], v[54:55]
	s_nop 1
	v_permlane16_swap_b32_e32 v48, v50
	v_permlane16_swap_b32_e32 v49, v51
	s_nop 0
	v_pk_add_f32 v[48:49], v[48:49], v[50:51]
	s_nop 0
	v_pk_add_f32 v[48:49], v[48:49], v[56:57]
	s_nop 0
	v_pk_mul_f32 v[48:49], v[48:49], s[12:13] op_sel_hi:[1,0]
	global_store_dwordx2 v46, v[48:49], s[4:5] nt
	s_endpgm
